# k_fine: final col store via the single generic loop (unrolled variants and size recomputation removed) on top of previous k_fine/agg2/stageA edits
# speedup vs baseline: 1.0821x; 1.0080x over previous
.LBB0_160:
	s_or_b64 exec, exec, s[0:1]
	s_waitcnt lgkmcnt(0)
	s_barrier
	s_and_saveexec_b64 s[0:1], vcc
	s_cbranch_execz .LBB0_175
	s_add_i32 s0, s44, s45
	s_add_i32 s0, s0, s47
	s_add_i32 s0, s0, s48
	s_add_i32 s0, s0, s49
	s_add_i32 s0, s0, s50
	s_add_i32 s0, s0, s51
	s_add_i32 s0, s0, s52
	s_add_i32 s0, s0, s53
	s_add_i32 s0, s0, s54
	s_add_i32 s0, s0, s55
	s_add_i32 s0, s0, s56
	s_add_i32 s0, s0, s57
	s_add_i32 s0, s0, s58
	s_add_i32 s1, s46, s33
	s_add_i32 s1, s1, s0
	v_add_u32_e32 v2, s1, v0
	v_lshlrev_b32_e32 v1, 2, v0
	s_mov_b64 s[0:1], 0
